# baseline (speedup 1.0000x reference)
_Z2kA5AArgs:
	s_load_dwordx2 s[34:35], s[0:1], 0x20
	s_load_dwordx16 s[16:31], s[0:1], 0x30
	s_lshl_b32 s3, s2, 3
	v_xor_b32_e32 v0, 0x100, v0
	s_nop 1
	v_readfirstlane_b32 s38, v0
	s_and_b32 s3, s3, 56
	s_ashr_i32 s4, s2, 5
	s_lshr_b32 s36, s38, 6
	s_add_i32 s3, s3, s4
	s_bfe_u32 s33, s2, 0x20003
	v_and_b32_e32 v1, 63, v0
	s_cmpk_gt_u32 s38, 0xff
	s_mov_b64 s[4:5], -1
	s_cbranch_scc1 .LBB0_3
	s_andn2_b64 vcc, exec, s[4:5]
	s_cbranch_vccz .LBB0_78
